# v30 + MoE gate/up epilogue re-emitted 8 elements at a time with packed f32 ops (same IEEE operations, no single-register dependency chain)
# speedup vs baseline: 1.0039x; 1.0022x over previous
; #define GAS __attribute__((address_space(1)))
;     __device__ __forceinline__ void operator()(const f32x4 (&acc)[2][2][4][2], const Unit& u, const float (&rs)[2][4], int wr, int wc, int fr, int fq) const {
;         unsigned char* tp = O + (size_t)u.pm * (BM * DEXP) + (size_t)(u.pn * 2 + (wc >> 1)) * (BM * 64) + (wr * 64 + fr) * 64 + (wc & 1) * 32 + 8 * fq;
; #pragma unroll
;         for (int ai = 0; ai < 2; ++ai)
; #pragma unroll
;             for (int m = 0; m < 4; ++m) { unsigned char* rowp = tp + (ai * HALF + m * 16) * 64;
;                 float o[8];
; #pragma unroll
;                 for (int n = 0; n < 2; ++n)
; #pragma unroll
;                     for (int j = 0; j < 4; ++j) { const float g = acc[ai][0][m][n][j], uu = acc[ai][1][m][n][j];
;                         const float sg = g * __builtin_amdgcn_rcpf(1.0f + __builtin_amdgcn_exp2f(-g * LOG2E)); o[n * 4 + j] = __builtin_amdgcn_fmed3f(sg * uu, -448.0f, 448.0f); }
;                 int p0 = __builtin_amdgcn_cvt_pk_fp8_f32(o[0], o[1], 0, false); p0 = __builtin_amdgcn_cvt_pk_fp8_f32(o[2], o[3], p0, true);
;                 int p1 = __builtin_amdgcn_cvt_pk_fp8_f32(o[4], o[5], 0, false); p1 = __builtin_amdgcn_cvt_pk_fp8_f32(o[6], o[7], p1, true);
;                 u32x2_t wv; wv.x = (unsigned)p0; wv.y = (unsigned)p1;
;                 *(GAS u32x2_t*)rowp = wv; }
.LBB0_1600:
	s_mov_b32 s100, 0xbfb8aa3b
	s_mov_b32 s101, 0xbfb8aa3b
	s_ashr_i32 s41, s40, 31
	s_lshl_b64 s[62:63], s[40:41], 16
	s_add_u32 s41, s87, s62
	s_addc_u32 s64, s88, s63
	s_lshl_b32 s62, s9, 1
	s_or_b32 s62, s62, s92
	s_ashr_i32 s63, s62, 31
	s_lshl_b64 s[62:63], s[62:63], 14
	s_add_u32 s62, s41, s62
	s_addc_u32 s63, s64, s63
	v_lshl_add_u64 v[4:5], s[62:63], 0, v[206:207]
	v_lshl_add_u64 v[4:5], v[4:5], 0, s[22:23]
	v_lshl_add_u64 v[4:5], v[4:5], 0, v[204:205]
	s_movk_i32 s41, 0x2000
	v_pk_mul_f32 v[230:231], v[192:193], s[100:101] op_sel_hi:[1,0]
	v_pk_mul_f32 v[234:235], v[194:195], s[100:101] op_sel_hi:[1,0]
	v_pk_mul_f32 v[236:237], v[188:189], s[100:101] op_sel_hi:[1,0]
	v_pk_mul_f32 v[248:249], v[190:191], s[100:101] op_sel_hi:[1,0]
	v_exp_f32_e32 v230, v230
	v_exp_f32_e32 v231, v231
	v_exp_f32_e32 v234, v234
	v_exp_f32_e32 v235, v235
	v_exp_f32_e32 v236, v236
	v_exp_f32_e32 v237, v237
	v_exp_f32_e32 v248, v248
	v_exp_f32_e32 v249, v249
	v_pk_add_f32 v[230:231], v[230:231], 1.0 op_sel_hi:[1,0]
	v_pk_add_f32 v[234:235], v[234:235], 1.0 op_sel_hi:[1,0]
	v_pk_add_f32 v[236:237], v[236:237], 1.0 op_sel_hi:[1,0]
	v_pk_add_f32 v[248:249], v[248:249], 1.0 op_sel_hi:[1,0]
	v_rcp_f32_e32 v230, v230
	v_rcp_f32_e32 v231, v231
	v_rcp_f32_e32 v234, v234
	v_rcp_f32_e32 v235, v235
	v_rcp_f32_e32 v236, v236
	v_rcp_f32_e32 v237, v237
	v_rcp_f32_e32 v248, v248
	v_rcp_f32_e32 v249, v249
	v_pk_mul_f32 v[230:231], v[192:193], v[230:231]
	v_pk_mul_f32 v[234:235], v[194:195], v[234:235]
	v_pk_mul_f32 v[236:237], v[188:189], v[236:237]
	v_pk_mul_f32 v[248:249], v[190:191], v[248:249]
	v_pk_mul_f32 v[230:231], v[160:161], v[230:231]
	v_pk_mul_f32 v[234:235], v[162:163], v[234:235]
	v_pk_mul_f32 v[236:237], v[156:157], v[236:237]
	v_pk_mul_f32 v[248:249], v[158:159], v[248:249]
	v_med3_f32 v7, v230, s4, v233
	v_med3_f32 v8, v231, s4, v233
	v_med3_f32 v9, v234, s4, v233
	v_med3_f32 v10, v235, s4, v233
	v_med3_f32 v11, v236, s4, v233
	v_med3_f32 v12, v237, s4, v233
	v_med3_f32 v13, v248, s4, v233
	v_med3_f32 v14, v249, s4, v233
	v_mov_b32_e32 v6, v3
	v_cvt_pk_fp8_f32 v6, v7, v8
	v_mov_b32_e32 v7, v3
	v_cvt_pk_fp8_f32 v7, v11, v12
	v_cvt_pk_fp8_f32 v6, v9, v10 op_sel:[0,0,1]
	v_cvt_pk_fp8_f32 v7, v13, v14 op_sel:[0,0,1]
	global_store_dwordx2 v[4:5], v[6:7], off
	v_pk_mul_f32 v[230:231], v[184:185], s[100:101] op_sel_hi:[1,0]
	v_pk_mul_f32 v[234:235], v[186:187], s[100:101] op_sel_hi:[1,0]
	v_pk_mul_f32 v[236:237], v[180:181], s[100:101] op_sel_hi:[1,0]
	v_pk_mul_f32 v[248:249], v[182:183], s[100:101] op_sel_hi:[1,0]
	v_exp_f32_e32 v230, v230
	v_exp_f32_e32 v231, v231
	v_exp_f32_e32 v234, v234
	v_exp_f32_e32 v235, v235
	v_exp_f32_e32 v236, v236
	v_exp_f32_e32 v237, v237
	v_exp_f32_e32 v248, v248
	v_exp_f32_e32 v249, v249
	v_pk_add_f32 v[230:231], v[230:231], 1.0 op_sel_hi:[1,0]
	v_pk_add_f32 v[234:235], v[234:235], 1.0 op_sel_hi:[1,0]
	v_pk_add_f32 v[236:237], v[236:237], 1.0 op_sel_hi:[1,0]
	v_pk_add_f32 v[248:249], v[248:249], 1.0 op_sel_hi:[1,0]
	v_rcp_f32_e32 v230, v230
	v_rcp_f32_e32 v231, v231
	v_rcp_f32_e32 v234, v234
	v_rcp_f32_e32 v235, v235
	v_rcp_f32_e32 v236, v236
	v_rcp_f32_e32 v237, v237
	v_rcp_f32_e32 v248, v248
	v_rcp_f32_e32 v249, v249
	v_pk_mul_f32 v[230:231], v[184:185], v[230:231]
	v_pk_mul_f32 v[234:235], v[186:187], v[234:235]
	v_pk_mul_f32 v[236:237], v[180:181], v[236:237]
	v_pk_mul_f32 v[248:249], v[182:183], v[248:249]
	v_pk_mul_f32 v[230:231], v[152:153], v[230:231]
	v_pk_mul_f32 v[234:235], v[154:155], v[234:235]
	v_pk_mul_f32 v[236:237], v[148:149], v[236:237]
	v_pk_mul_f32 v[248:249], v[150:151], v[248:249]
	v_med3_f32 v7, v230, s4, v233
	v_med3_f32 v8, v231, s4, v233
	v_med3_f32 v9, v234, s4, v233
	v_med3_f32 v10, v235, s4, v233
	v_med3_f32 v11, v236, s4, v233
	v_med3_f32 v12, v237, s4, v233
	v_med3_f32 v13, v248, s4, v233
	v_med3_f32 v14, v249, s4, v233
	v_mov_b32_e32 v6, v3
	v_cvt_pk_fp8_f32 v6, v7, v8
	v_mov_b32_e32 v7, v3
	v_cvt_pk_fp8_f32 v7, v11, v12
	v_cvt_pk_fp8_f32 v6, v9, v10 op_sel:[0,0,1]
	v_cvt_pk_fp8_f32 v7, v13, v14 op_sel:[0,0,1]
	global_store_dwordx2 v[4:5], v[6:7], off offset:1024
	v_pk_mul_f32 v[230:231], v[176:177], s[100:101] op_sel_hi:[1,0]
	v_pk_mul_f32 v[234:235], v[178:179], s[100:101] op_sel_hi:[1,0]
	v_pk_mul_f32 v[236:237], v[172:173], s[100:101] op_sel_hi:[1,0]
	v_pk_mul_f32 v[248:249], v[174:175], s[100:101] op_sel_hi:[1,0]
	v_exp_f32_e32 v230, v230
	v_exp_f32_e32 v231, v231
	v_exp_f32_e32 v234, v234
	v_exp_f32_e32 v235, v235
	v_exp_f32_e32 v236, v236
	v_exp_f32_e32 v237, v237
	v_exp_f32_e32 v248, v248
	v_exp_f32_e32 v249, v249
	v_pk_add_f32 v[230:231], v[230:231], 1.0 op_sel_hi:[1,0]
	v_pk_add_f32 v[234:235], v[234:235], 1.0 op_sel_hi:[1,0]
	v_pk_add_f32 v[236:237], v[236:237], 1.0 op_sel_hi:[1,0]
	v_pk_add_f32 v[248:249], v[248:249], 1.0 op_sel_hi:[1,0]
	v_rcp_f32_e32 v230, v230
	v_rcp_f32_e32 v231, v231
	v_rcp_f32_e32 v234, v234
	v_rcp_f32_e32 v235, v235
	v_rcp_f32_e32 v236, v236
	v_rcp_f32_e32 v237, v237
	v_rcp_f32_e32 v248, v248
	v_rcp_f32_e32 v249, v249
	v_pk_mul_f32 v[230:231], v[176:177], v[230:231]
	v_pk_mul_f32 v[234:235], v[178:179], v[234:235]
	v_pk_mul_f32 v[236:237], v[172:173], v[236:237]
	v_pk_mul_f32 v[248:249], v[174:175], v[248:249]
	v_pk_mul_f32 v[230:231], v[144:145], v[230:231]
	v_pk_mul_f32 v[234:235], v[146:147], v[234:235]
	v_pk_mul_f32 v[236:237], v[140:141], v[236:237]
	v_pk_mul_f32 v[248:249], v[142:143], v[248:249]
	v_med3_f32 v7, v230, s4, v233
	v_med3_f32 v8, v231, s4, v233
	v_med3_f32 v9, v234, s4, v233
	v_med3_f32 v10, v235, s4, v233
	v_med3_f32 v11, v236, s4, v233
	v_med3_f32 v12, v237, s4, v233
	v_med3_f32 v13, v248, s4, v233
	v_med3_f32 v14, v249, s4, v233
; #define GAS __attribute__((address_space(1)))
;     __device__ __forceinline__ void operator()(const f32x4 (&acc)[2][2][4][2], const Unit& u, const float (&rs)[2][4], int wr, int wc, int fr, int fq) const {
;         unsigned char* tp = O + (size_t)u.pm * (BM * DEXP) + (size_t)(u.pn * 2 + (wc >> 1)) * (BM * 64) + (wr * 64 + fr) * 64 + (wc & 1) * 32 + 8 * fq;
; #pragma unroll
;         for (int ai = 0; ai < 2; ++ai)
; #pragma unroll
;             for (int m = 0; m < 4; ++m) { unsigned char* rowp = tp + (ai * HALF + m * 16) * 64;
;                 float o[8];
; #pragma unroll
;                 for (int n = 0; n < 2; ++n)
; #pragma unroll
;                     for (int j = 0; j < 4; ++j) { const float g = acc[ai][0][m][n][j], uu = acc[ai][1][m][n][j];
;                         const float sg = g * __builtin_amdgcn_rcpf(1.0f + __builtin_amdgcn_exp2f(-g * LOG2E)); o[n * 4 + j] = __builtin_amdgcn_fmed3f(sg * uu, -448.0f, 448.0f); }
;                 int p0 = __builtin_amdgcn_cvt_pk_fp8_f32(o[0], o[1], 0, false); p0 = __builtin_amdgcn_cvt_pk_fp8_f32(o[2], o[3], p0, true);
;                 int p1 = __builtin_amdgcn_cvt_pk_fp8_f32(o[4], o[5], 0, false); p1 = __builtin_amdgcn_cvt_pk_fp8_f32(o[6], o[7], p1, true);
;                 u32x2_t wv; wv.x = (unsigned)p0; wv.y = (unsigned)p1;
;                 *(GAS u32x2_t*)rowp = wv; }
	v_mov_b32_e32 v6, v3
	v_cvt_pk_fp8_f32 v6, v7, v8
	v_mov_b32_e32 v7, v3
	v_cvt_pk_fp8_f32 v7, v11, v12
	v_cvt_pk_fp8_f32 v6, v9, v10 op_sel:[0,0,1]
	v_cvt_pk_fp8_f32 v7, v13, v14 op_sel:[0,0,1]
	global_store_dwordx2 v[4:5], v[6:7], off offset:2048
	v_pk_mul_f32 v[230:231], v[168:169], s[100:101] op_sel_hi:[1,0]
	v_pk_mul_f32 v[234:235], v[170:171], s[100:101] op_sel_hi:[1,0]
	v_pk_mul_f32 v[236:237], v[164:165], s[100:101] op_sel_hi:[1,0]
	v_pk_mul_f32 v[248:249], v[166:167], s[100:101] op_sel_hi:[1,0]
	v_exp_f32_e32 v230, v230
	v_exp_f32_e32 v231, v231
	v_exp_f32_e32 v234, v234
	v_exp_f32_e32 v235, v235
	v_exp_f32_e32 v236, v236
	v_exp_f32_e32 v237, v237
	v_exp_f32_e32 v248, v248
	v_exp_f32_e32 v249, v249
	v_pk_add_f32 v[230:231], v[230:231], 1.0 op_sel_hi:[1,0]
	v_pk_add_f32 v[234:235], v[234:235], 1.0 op_sel_hi:[1,0]
	v_pk_add_f32 v[236:237], v[236:237], 1.0 op_sel_hi:[1,0]
	v_pk_add_f32 v[248:249], v[248:249], 1.0 op_sel_hi:[1,0]
	v_rcp_f32_e32 v230, v230
	v_rcp_f32_e32 v231, v231
	v_rcp_f32_e32 v234, v234
	v_rcp_f32_e32 v235, v235
	v_rcp_f32_e32 v236, v236
	v_rcp_f32_e32 v237, v237
	v_rcp_f32_e32 v248, v248
	v_rcp_f32_e32 v249, v249
	v_pk_mul_f32 v[230:231], v[168:169], v[230:231]
	v_pk_mul_f32 v[234:235], v[170:171], v[234:235]
	v_pk_mul_f32 v[236:237], v[164:165], v[236:237]
	v_pk_mul_f32 v[248:249], v[166:167], v[248:249]
	v_pk_mul_f32 v[230:231], v[136:137], v[230:231]
	v_pk_mul_f32 v[234:235], v[138:139], v[234:235]
	v_pk_mul_f32 v[236:237], v[132:133], v[236:237]
	v_pk_mul_f32 v[248:249], v[134:135], v[248:249]
	v_med3_f32 v7, v230, s4, v233
	v_med3_f32 v8, v231, s4, v233
	v_med3_f32 v9, v234, s4, v233
	v_med3_f32 v10, v235, s4, v233
	v_med3_f32 v11, v236, s4, v233
	v_med3_f32 v12, v237, s4, v233
	v_med3_f32 v13, v248, s4, v233
	v_med3_f32 v14, v249, s4, v233
	v_mov_b32_e32 v6, v3
	v_cvt_pk_fp8_f32 v6, v7, v8
	v_mov_b32_e32 v7, v3
	v_cvt_pk_fp8_f32 v7, v11, v12
	v_cvt_pk_fp8_f32 v6, v9, v10 op_sel:[0,0,1]
	v_cvt_pk_fp8_f32 v7, v13, v14 op_sel:[0,0,1]
	global_store_dwordx2 v[4:5], v[6:7], off offset:3072
	v_add_co_u32_e32 v4, vcc, s41, v4
	s_nop 1
	v_addc_co_u32_e32 v5, vcc, 0, v5, vcc
	s_and_b64 vcc, exec, s[38:39]
	v_pk_mul_f32 v[230:231], v[128:129], s[100:101] op_sel_hi:[1,0]
	v_pk_mul_f32 v[234:235], v[130:131], s[100:101] op_sel_hi:[1,0]
	v_pk_mul_f32 v[236:237], v[124:125], s[100:101] op_sel_hi:[1,0]
	v_pk_mul_f32 v[248:249], v[126:127], s[100:101] op_sel_hi:[1,0]
	v_exp_f32_e32 v230, v230
	v_exp_f32_e32 v231, v231
	v_exp_f32_e32 v234, v234
	v_exp_f32_e32 v235, v235
	v_exp_f32_e32 v236, v236
	v_exp_f32_e32 v237, v237
	v_exp_f32_e32 v248, v248
	v_exp_f32_e32 v249, v249
	v_pk_add_f32 v[230:231], v[230:231], 1.0 op_sel_hi:[1,0]
	v_pk_add_f32 v[234:235], v[234:235], 1.0 op_sel_hi:[1,0]
	v_pk_add_f32 v[236:237], v[236:237], 1.0 op_sel_hi:[1,0]
	v_pk_add_f32 v[248:249], v[248:249], 1.0 op_sel_hi:[1,0]
	v_rcp_f32_e32 v230, v230
	v_rcp_f32_e32 v231, v231
	v_rcp_f32_e32 v234, v234
	v_rcp_f32_e32 v235, v235
	v_rcp_f32_e32 v236, v236
	v_rcp_f32_e32 v237, v237
	v_rcp_f32_e32 v248, v248
	v_rcp_f32_e32 v249, v249
	v_pk_mul_f32 v[230:231], v[128:129], v[230:231]
	v_pk_mul_f32 v[234:235], v[130:131], v[234:235]
	v_pk_mul_f32 v[236:237], v[124:125], v[236:237]
	v_pk_mul_f32 v[248:249], v[126:127], v[248:249]
	v_pk_mul_f32 v[230:231], v[96:97], v[230:231]
	v_pk_mul_f32 v[234:235], v[98:99], v[234:235]
	v_pk_mul_f32 v[236:237], v[92:93], v[236:237]
	v_pk_mul_f32 v[248:249], v[94:95], v[248:249]
	v_med3_f32 v7, v230, s4, v233
	v_med3_f32 v8, v231, s4, v233
	v_med3_f32 v9, v234, s4, v233
	v_med3_f32 v10, v235, s4, v233
	v_med3_f32 v11, v236, s4, v233
	v_med3_f32 v12, v237, s4, v233
	v_med3_f32 v13, v248, s4, v233
	v_med3_f32 v14, v249, s4, v233
	v_mov_b32_e32 v6, v3
	v_cvt_pk_fp8_f32 v6, v7, v8
	v_mov_b32_e32 v7, v3
	v_cvt_pk_fp8_f32 v7, v11, v12
	v_cvt_pk_fp8_f32 v6, v9, v10 op_sel:[0,0,1]
	v_cvt_pk_fp8_f32 v7, v13, v14 op_sel:[0,0,1]
	global_store_dwordx2 v[4:5], v[6:7], off
	v_pk_mul_f32 v[230:231], v[120:121], s[100:101] op_sel_hi:[1,0]
	v_pk_mul_f32 v[234:235], v[122:123], s[100:101] op_sel_hi:[1,0]
	v_pk_mul_f32 v[236:237], v[116:117], s[100:101] op_sel_hi:[1,0]
	v_pk_mul_f32 v[248:249], v[118:119], s[100:101] op_sel_hi:[1,0]
	v_exp_f32_e32 v230, v230
	v_exp_f32_e32 v231, v231
	v_exp_f32_e32 v234, v234
	v_exp_f32_e32 v235, v235
	v_exp_f32_e32 v236, v236
	v_exp_f32_e32 v237, v237
	v_exp_f32_e32 v248, v248
	v_exp_f32_e32 v249, v249
	v_pk_add_f32 v[230:231], v[230:231], 1.0 op_sel_hi:[1,0]
	v_pk_add_f32 v[234:235], v[234:235], 1.0 op_sel_hi:[1,0]
	v_pk_add_f32 v[236:237], v[236:237], 1.0 op_sel_hi:[1,0]
	v_pk_add_f32 v[248:249], v[248:249], 1.0 op_sel_hi:[1,0]
	v_rcp_f32_e32 v230, v230
	v_rcp_f32_e32 v231, v231
	v_rcp_f32_e32 v234, v234
; #define GAS __attribute__((address_space(1)))
; #define PG8_BAR __builtin_amdgcn_s_barrier()
; template <class Epi, class Sched>
; __device__ __forceinline__ void gemm_phase(const int tid, LAS unsigned char* lds, const char* Abase, const int lda, const int ldb, const int K, const Sched& S, const Epi& E) {
;     ...
;         cur = nxt; cB = nB; cA = nA; ++ui;
;         if (wr == 1) PG8_BAR;
;     __device__ __forceinline__ void operator()(const f32x4 (&acc)[2][2][4][2], const Unit& u, const float (&rs)[2][4], int wr, int wc, int fr, int fq) const {
;         unsigned char* tp = O + (size_t)u.pm * (BM * DEXP) + (size_t)(u.pn * 2 + (wc >> 1)) * (BM * 64) + (wr * 64 + fr) * 64 + (wc & 1) * 32 + 8 * fq;
; #pragma unroll
;         for (int ai = 0; ai < 2; ++ai)
; #pragma unroll
;             for (int m = 0; m < 4; ++m) { unsigned char* rowp = tp + (ai * HALF + m * 16) * 64;
;                 float o[8];
; #pragma unroll
;                 for (int n = 0; n < 2; ++n)
; #pragma unroll
;                     for (int j = 0; j < 4; ++j) { const float g = acc[ai][0][m][n][j], uu = acc[ai][1][m][n][j];
;                         const float sg = g * __builtin_amdgcn_rcpf(1.0f + __builtin_amdgcn_exp2f(-g * LOG2E)); o[n * 4 + j] = __builtin_amdgcn_fmed3f(sg * uu, -448.0f, 448.0f); }
;                 int p0 = __builtin_amdgcn_cvt_pk_fp8_f32(o[0], o[1], 0, false); p0 = __builtin_amdgcn_cvt_pk_fp8_f32(o[2], o[3], p0, true);
;                 int p1 = __builtin_amdgcn_cvt_pk_fp8_f32(o[4], o[5], 0, false); p1 = __builtin_amdgcn_cvt_pk_fp8_f32(o[6], o[7], p1, true);
;                 u32x2_t wv; wv.x = (unsigned)p0; wv.y = (unsigned)p1;
;                 *(GAS u32x2_t*)rowp = wv; }
	v_rcp_f32_e32 v235, v235
	v_rcp_f32_e32 v236, v236
	v_rcp_f32_e32 v237, v237
	v_rcp_f32_e32 v248, v248
	v_rcp_f32_e32 v249, v249
	v_pk_mul_f32 v[230:231], v[120:121], v[230:231]
	v_pk_mul_f32 v[234:235], v[122:123], v[234:235]
	v_pk_mul_f32 v[236:237], v[116:117], v[236:237]
	v_pk_mul_f32 v[248:249], v[118:119], v[248:249]
	v_pk_mul_f32 v[230:231], v[88:89], v[230:231]
	v_pk_mul_f32 v[234:235], v[90:91], v[234:235]
	v_pk_mul_f32 v[236:237], v[84:85], v[236:237]
	v_pk_mul_f32 v[248:249], v[86:87], v[248:249]
	v_med3_f32 v7, v230, s4, v233
	v_med3_f32 v8, v231, s4, v233
	v_med3_f32 v9, v234, s4, v233
	v_med3_f32 v10, v235, s4, v233
	v_med3_f32 v11, v236, s4, v233
	v_med3_f32 v12, v237, s4, v233
	v_med3_f32 v13, v248, s4, v233
	v_med3_f32 v14, v249, s4, v233
	v_mov_b32_e32 v6, v3
	v_cvt_pk_fp8_f32 v6, v7, v8
	v_mov_b32_e32 v7, v3
	v_cvt_pk_fp8_f32 v7, v11, v12
	v_cvt_pk_fp8_f32 v6, v9, v10 op_sel:[0,0,1]
	v_cvt_pk_fp8_f32 v7, v13, v14 op_sel:[0,0,1]
	global_store_dwordx2 v[4:5], v[6:7], off offset:1024
	v_pk_mul_f32 v[230:231], v[112:113], s[100:101] op_sel_hi:[1,0]
	v_pk_mul_f32 v[234:235], v[114:115], s[100:101] op_sel_hi:[1,0]
	v_pk_mul_f32 v[236:237], v[108:109], s[100:101] op_sel_hi:[1,0]
	v_pk_mul_f32 v[248:249], v[110:111], s[100:101] op_sel_hi:[1,0]
	v_exp_f32_e32 v230, v230
	v_exp_f32_e32 v231, v231
	v_exp_f32_e32 v234, v234
	v_exp_f32_e32 v235, v235
	v_exp_f32_e32 v236, v236
	v_exp_f32_e32 v237, v237
	v_exp_f32_e32 v248, v248
	v_exp_f32_e32 v249, v249
	v_pk_add_f32 v[230:231], v[230:231], 1.0 op_sel_hi:[1,0]
	v_pk_add_f32 v[234:235], v[234:235], 1.0 op_sel_hi:[1,0]
	v_pk_add_f32 v[236:237], v[236:237], 1.0 op_sel_hi:[1,0]
	v_pk_add_f32 v[248:249], v[248:249], 1.0 op_sel_hi:[1,0]
	v_rcp_f32_e32 v230, v230
	v_rcp_f32_e32 v231, v231
	v_rcp_f32_e32 v234, v234
	v_rcp_f32_e32 v235, v235
	v_rcp_f32_e32 v236, v236
	v_rcp_f32_e32 v237, v237
	v_rcp_f32_e32 v248, v248
	v_rcp_f32_e32 v249, v249
	v_pk_mul_f32 v[230:231], v[112:113], v[230:231]
	v_pk_mul_f32 v[234:235], v[114:115], v[234:235]
	v_pk_mul_f32 v[236:237], v[108:109], v[236:237]
	v_pk_mul_f32 v[248:249], v[110:111], v[248:249]
	v_pk_mul_f32 v[230:231], v[80:81], v[230:231]
	v_pk_mul_f32 v[234:235], v[82:83], v[234:235]
	v_pk_mul_f32 v[236:237], v[76:77], v[236:237]
	v_pk_mul_f32 v[248:249], v[78:79], v[248:249]
	v_med3_f32 v7, v230, s4, v233
	v_med3_f32 v8, v231, s4, v233
	v_med3_f32 v9, v234, s4, v233
	v_med3_f32 v10, v235, s4, v233
	v_med3_f32 v11, v236, s4, v233
	v_med3_f32 v12, v237, s4, v233
	v_med3_f32 v13, v248, s4, v233
	v_med3_f32 v14, v249, s4, v233
	v_mov_b32_e32 v6, v3
	v_cvt_pk_fp8_f32 v6, v7, v8
	v_mov_b32_e32 v7, v3
	v_cvt_pk_fp8_f32 v7, v11, v12
	v_cvt_pk_fp8_f32 v6, v9, v10 op_sel:[0,0,1]
	v_cvt_pk_fp8_f32 v7, v13, v14 op_sel:[0,0,1]
	global_store_dwordx2 v[4:5], v[6:7], off offset:2048
	v_pk_mul_f32 v[230:231], v[104:105], s[100:101] op_sel_hi:[1,0]
	v_pk_mul_f32 v[234:235], v[106:107], s[100:101] op_sel_hi:[1,0]
	v_pk_mul_f32 v[236:237], v[100:101], s[100:101] op_sel_hi:[1,0]
	v_pk_mul_f32 v[248:249], v[102:103], s[100:101] op_sel_hi:[1,0]
	v_exp_f32_e32 v230, v230
	v_exp_f32_e32 v231, v231
	v_exp_f32_e32 v234, v234
	v_exp_f32_e32 v235, v235
	v_exp_f32_e32 v236, v236
	v_exp_f32_e32 v237, v237
	v_exp_f32_e32 v248, v248
	v_exp_f32_e32 v249, v249
	v_pk_add_f32 v[230:231], v[230:231], 1.0 op_sel_hi:[1,0]
	v_pk_add_f32 v[234:235], v[234:235], 1.0 op_sel_hi:[1,0]
	v_pk_add_f32 v[236:237], v[236:237], 1.0 op_sel_hi:[1,0]
	v_pk_add_f32 v[248:249], v[248:249], 1.0 op_sel_hi:[1,0]
	v_rcp_f32_e32 v230, v230
	v_rcp_f32_e32 v231, v231
	v_rcp_f32_e32 v234, v234
	v_rcp_f32_e32 v235, v235
	v_rcp_f32_e32 v236, v236
	v_rcp_f32_e32 v237, v237
	v_rcp_f32_e32 v248, v248
	v_rcp_f32_e32 v249, v249
	v_pk_mul_f32 v[230:231], v[104:105], v[230:231]
	v_pk_mul_f32 v[234:235], v[106:107], v[234:235]
	v_pk_mul_f32 v[236:237], v[100:101], v[236:237]
	v_pk_mul_f32 v[248:249], v[102:103], v[248:249]
	v_pk_mul_f32 v[230:231], v[72:73], v[230:231]
	v_pk_mul_f32 v[234:235], v[74:75], v[234:235]
	v_pk_mul_f32 v[236:237], v[68:69], v[236:237]
	v_pk_mul_f32 v[248:249], v[70:71], v[248:249]
	v_med3_f32 v7, v230, s4, v233
	v_med3_f32 v8, v231, s4, v233
	v_med3_f32 v9, v234, s4, v233
	v_med3_f32 v10, v235, s4, v233
	v_med3_f32 v11, v236, s4, v233
	v_med3_f32 v12, v237, s4, v233
	v_med3_f32 v13, v248, s4, v233
	v_med3_f32 v14, v249, s4, v233
	v_mov_b32_e32 v6, v3
	v_cvt_pk_fp8_f32 v6, v7, v8
	v_mov_b32_e32 v7, v3
	v_cvt_pk_fp8_f32 v7, v11, v12
	v_cvt_pk_fp8_f32 v6, v9, v10 op_sel:[0,0,1]
	v_cvt_pk_fp8_f32 v7, v13, v14 op_sel:[0,0,1]
	global_store_dwordx2 v[4:5], v[6:7], off offset:3072
	s_cbranch_vccnz .LBB0_1566
	s_andn2_b64 vcc, exec, s[48:49]
	s_cbranch_vccnz .LBB0_1565
	s_barrier
	s_branch .LBB0_1565

; __global__ void __launch_bounds__(NWAVES * 64, 2) mk_fwd(Args args) {
	.amdhsa_kernel _Z6mk_fwd4Args
		.amdhsa_group_segment_fixed_size 0
		.amdhsa_private_segment_fixed_size 0
		.amdhsa_kernarg_size 440
		.amdhsa_user_sgpr_count 2
		.amdhsa_user_sgpr_dispatch_ptr 0
		.amdhsa_user_sgpr_queue_ptr 0
		.amdhsa_user_sgpr_kernarg_segment_ptr 1
		.amdhsa_user_sgpr_dispatch_id 0
		.amdhsa_user_sgpr_kernarg_preload_length 0
		.amdhsa_user_sgpr_kernarg_preload_offset 0
		.amdhsa_user_sgpr_private_segment_size 0
		.amdhsa_uses_dynamic_stack 0
		.amdhsa_enable_private_segment 0
		.amdhsa_system_sgpr_workgroup_id_x 1
		.amdhsa_system_sgpr_workgroup_id_y 0
		.amdhsa_system_sgpr_workgroup_id_z 0
		.amdhsa_system_sgpr_workgroup_info 0
		.amdhsa_system_vgpr_workitem_id 0
		.amdhsa_next_free_vgpr 256
		.amdhsa_next_free_sgpr 102
		.amdhsa_accum_offset 256
		.amdhsa_reserve_vcc 1
		.amdhsa_float_round_mode_32 0
		.amdhsa_float_round_mode_16_64 0
		.amdhsa_float_denorm_mode_32 3
		.amdhsa_float_denorm_mode_16_64 3
		.amdhsa_dx10_clamp 1
		.amdhsa_ieee_mode 1
		.amdhsa_fp16_overflow 0
		.amdhsa_tg_split 0
		.amdhsa_exception_fp_ieee_invalid_op 0
		.amdhsa_exception_fp_denorm_src 0
		.amdhsa_exception_fp_ieee_div_zero 0
		.amdhsa_exception_fp_ieee_overflow 0
		.amdhsa_exception_fp_ieee_underflow 0
		.amdhsa_exception_fp_ieee_inexact 0
		.amdhsa_exception_int_div_zero 0
	.end_amdhsa_kernel

; __global__ void __launch_bounds__(NWAVES * 64, 2) mk_fwd(Args args) {
amdhsa.kernels:
  - .agpr_count:     0
    .args:
      - .offset:         0
        .size:           184
        .value_kind:     by_value
      - .offset:         184
        .size:           4
        .value_kind:     hidden_block_count_x
      - .offset:         188
        .size:           4
        .value_kind:     hidden_block_count_y
      - .offset:         192
        .size:           4
        .value_kind:     hidden_block_count_z
      - .offset:         196
        .size:           2
        .value_kind:     hidden_group_size_x
      - .offset:         198
        .size:           2
        .value_kind:     hidden_group_size_y
      - .offset:         200
        .size:           2
        .value_kind:     hidden_group_size_z
      - .offset:         202
        .size:           2
        .value_kind:     hidden_remainder_x
      - .offset:         204
        .size:           2
        .value_kind:     hidden_remainder_y
      - .offset:         206
        .size:           2
        .value_kind:     hidden_remainder_z
      - .offset:         224
        .size:           8
        .value_kind:     hidden_global_offset_x
      - .offset:         232
        .size:           8
        .value_kind:     hidden_global_offset_y
      - .offset:         240
        .size:           8
        .value_kind:     hidden_global_offset_z
      - .offset:         248
        .size:           2
        .value_kind:     hidden_grid_dims
      - .offset:         304
        .size:           4
        .value_kind:     hidden_dynamic_lds_size
    .group_segment_fixed_size: 0
    .kernarg_segment_align: 8
    .kernarg_segment_size: 440
    .language:       OpenCL C
    .language_version:
      - 2
      - 0
    .max_flat_workgroup_size: 512
    .name:           _Z6mk_fwd4Args
    .private_segment_fixed_size: 0
    .sgpr_count:     108
    .sgpr_spill_count: 225
    .symbol:         _Z6mk_fwd4Args.kd
    .uniform_work_group_size: 1
    .uses_dynamic_stack: false
    .vgpr_count:     256
    .vgpr_spill_count: 0
    .wavefront_size: 64
